# v47 + router phase prologue: the 8 serial w_router load->wait->LDS-write round trips per thread issued together
# speedup vs baseline: 1.0159x; 1.0111x over previous
.LBB0_1688:
	ds_read_b32 v8, v6
	ds_read_b32 v9, v7
	s_waitcnt lgkmcnt(1)
	v_readfirstlane_b32 s12, v8
	s_waitcnt lgkmcnt(0)
	v_readfirstlane_b32 s13, v9
	s_nop 1
	v_lshl_add_u64 v[8:9], s[12:13], 0, v[2:3]
	global_load_dwordx4 v[100:103], v[8:9], off
	v_lshl_add_u64 v[8:9], v[8:9], 0, s[8:9]
	global_load_dwordx4 v[104:107], v[8:9], off
	v_lshl_add_u64 v[8:9], v[8:9], 0, s[8:9]
	global_load_dwordx4 v[108:111], v[8:9], off
	v_lshl_add_u64 v[8:9], v[8:9], 0, s[8:9]
	global_load_dwordx4 v[112:115], v[8:9], off
	v_lshl_add_u64 v[8:9], v[8:9], 0, s[8:9]
	global_load_dwordx4 v[116:119], v[8:9], off
	v_lshl_add_u64 v[8:9], v[8:9], 0, s[8:9]
	global_load_dwordx4 v[120:123], v[8:9], off
	v_lshl_add_u64 v[8:9], v[8:9], 0, s[8:9]
	global_load_dwordx4 v[124:127], v[8:9], off
	v_lshl_add_u64 v[8:9], v[8:9], 0, s[8:9]
	global_load_dwordx4 v[128:131], v[8:9], off
	s_waitcnt vmcnt(7)
	ds_write_b128 v5, v[100:103]
	s_waitcnt vmcnt(6)
	ds_write_b128 v5, v[104:107] offset:8192
	s_waitcnt vmcnt(5)
	ds_write_b128 v5, v[108:111] offset:16384
	s_waitcnt vmcnt(4)
	ds_write_b128 v5, v[112:115] offset:24576
	s_waitcnt vmcnt(3)
	ds_write_b128 v5, v[116:119] offset:32768
	s_waitcnt vmcnt(2)
	ds_write_b128 v5, v[120:123] offset:40960
	s_waitcnt vmcnt(1)
	ds_write_b128 v5, v[124:127] offset:49152
	s_waitcnt vmcnt(0)
	ds_write_b128 v5, v[128:131] offset:57344
